# speedup vs baseline: 1.0116x; 1.0039x over previous
.LBB0_6:
	s_addk_i32 s8, 0x400
	s_waitcnt vmcnt(1)
	v_cvt_pk_bf16_f32 v6, v6, v14
	v_mul_u32_u24_e32 v14, 0x420, v22
	s_lshr_b32 s4, s8, 6
	s_mov_b32 s5, 0
	v_lshl_add_u32 v14, v1, 2, v14
	s_waitcnt vmcnt(0)
	v_cvt_pk_bf16_f32 v2, v2, v10
	v_cvt_pk_bf16_f32 v3, v3, v11
	s_lshl_b64 s[4:5], s[4:5], 17
	ds_write2_b32 v14, v2, v3 offset0:132 offset1:165
	v_cvt_pk_bf16_f32 v2, v4, v12
	s_add_u32 s4, s6, s4
	v_mul_u32_u24_e32 v4, 0x84, v1
	v_cvt_pk_bf16_f32 v7, v7, v15
	v_cvt_pk_bf16_f32 v3, v5, v13
	s_addc_u32 s5, s7, s5
	v_mov_b32_e32 v19, 0
	v_lshl_add_u32 v4, v22, 4, v4
	ds_write2_b32 v14, v6, v7 offset1:33
	v_cvt_pk_bf16_f32 v6, v8, v16
	v_cvt_pk_bf16_f32 v7, v9, v17
	ds_write2_b32 v14, v2, v3 offset0:198 offset1:231
	v_lshl_add_u64 v[2:3], s[4:5], 0, v[18:19]
	v_add_lshl_u32 v18, s3, v1, 7
	v_add_u32_e32 v1, 0x1080, v4
	ds_write2_b32 v14, v6, v7 offset0:66 offset1:99
	s_waitcnt lgkmcnt(0)
	s_barrier
	ds_read2_b32 v[6:7], v4 offset1:1
	ds_read2_b32 v[8:9], v4 offset0:2 offset1:3
	v_add_u32_e32 v4, 0x1088, v4
	ds_read2_b32 v[10:11], v1 offset1:1
	ds_read2_b32 v[12:13], v4 offset1:1
	v_lshl_add_u64 v[4:5], v[2:3], 0, v[18:19]
	v_add_u32_e32 v18, 0x1000, v18
	v_lshl_add_u64 v[2:3], v[2:3], 0, v[18:19]
	s_waitcnt lgkmcnt(2)
	global_store_dwordx4 v[4:5], v[6:9], off nt
	s_waitcnt lgkmcnt(0)
	global_store_dwordx4 v[2:3], v[10:13], off nt
	s_mov_b64 s[4:5], 0
